# v82 + grid barrier: the workgroup completing the top-level count adds to every XCD's local generation word itself (with the top-level generation add); other XCD leaders no longer forward the release (
# baseline (speedup 1.0000x reference)
; __device__ __forceinline__ unsigned xb_ld(unsigned* p)              { return __hip_atomic_load(p, __ATOMIC_RELAXED, __HIP_MEMORY_SCOPE_AGENT); }
; __device__ __forceinline__ unsigned xb_add(unsigned* p, unsigned v) { return __hip_atomic_fetch_add(p, v, __ATOMIC_RELAXED, __HIP_MEMORY_SCOPE_AGENT); }
; #define XB_SPIN(cond, bar) do { unsigned _sp = 0; while (cond) { __builtin_amdgcn_s_sleep(1); \
;     if ((++_sp & 255u) == 0u) { if (xb_ld(&(bar)[XB_TMO])) break; if (_sp > XB_SPIN_CAP) { atomicAdd(&(bar)[XB_TMO], 1u); break; } } } } while (0)
; __device__ __forceinline__ void xcd_barrier(const XcdBarrier& b) {
;     ...
;             const unsigned og = xb_add(&bar[XB_TOP], 1u);
;             const unsigned tg = og / nx;
;             if (og + 1u == (tg + 1u) * nx) xb_add(&bar[XB_TOPGEN], 1u);
;             else XB_SPIN(xb_ld(&bar[XB_TOPGEN]) == tg, bar);
;             __builtin_amdgcn_fence(__ATOMIC_ACQUIRE, "agent");
;             xb_add(&bar[XB_XGEN(b.x)], 1u);
;             asm volatile("s_waitcnt vmcnt(0)" ::: "memory");
.LBB0_237:
	s_or_b64 exec, exec, s[10:11]
	s_and_saveexec_b64 s[10:11], s[14:15]
	s_cbranch_execz .LBB0_239
	v_mov_b32_e32 v1, 1
	global_atomic_add v[2:3], v1, off
	v_mov_b32_e32 v2, 0x2400
	global_atomic_add v2, v1, s[90:91]
	v_mov_b32_e32 v2, 0x2500
	global_atomic_add v2, v1, s[90:91]
	v_mov_b32_e32 v2, 0x2600
	global_atomic_add v2, v1, s[90:91]
	v_mov_b32_e32 v2, 0x2700
	global_atomic_add v2, v1, s[90:91]
	v_mov_b32_e32 v2, 0x2800
	global_atomic_add v2, v1, s[90:91]
	v_mov_b32_e32 v2, 0x2900
	global_atomic_add v2, v1, s[90:91]
	v_mov_b32_e32 v2, 0x2a00
	global_atomic_add v2, v1, s[90:91]
	v_mov_b32_e32 v2, 0x2b00
	global_atomic_add v2, v1, s[90:91]
	v_mov_b32_e32 v2, 0x2c00
	global_atomic_add v2, v1, s[90:91]
	v_mov_b32_e32 v2, 0x2d00
	global_atomic_add v2, v1, s[90:91]
	v_mov_b32_e32 v2, 0x2e00
	global_atomic_add v2, v1, s[90:91]
	v_mov_b32_e32 v2, 0x2f00
	global_atomic_add v2, v1, s[90:91]
	v_mov_b32_e32 v2, 0x3000
	global_atomic_add v2, v1, s[90:91]
	v_mov_b32_e32 v2, 0x3100
	global_atomic_add v2, v1, s[90:91]
	v_mov_b32_e32 v2, 0x3200
	global_atomic_add v2, v1, s[90:91]
	v_mov_b32_e32 v2, 0x3300
	global_atomic_add v2, v1, s[90:91]
.LBB0_239:
	s_or_b64 exec, exec, s[10:11]
	s_mov_b64 s[10:11], exec
	v_mbcnt_lo_u32_b32 v1, s10, 0
	v_mbcnt_hi_u32_b32 v1, s11, v1
	v_cmp_eq_u32_e32 vcc, 0, v1
	s_and_saveexec_b64 s[12:13], vcc
	s_cbranch_execz .LBB0_241
	s_bcnt1_i32_b64 s2, s[10:11]
	v_mov_b32_e32 v1, 0x2000
	v_mov_b32_e32 v2, s2
.LBB0_241:
	s_or_b64 exec, exec, s[12:13]

; __device__ __forceinline__ unsigned xb_ld(unsigned* p)              { return __hip_atomic_load(p, __ATOMIC_RELAXED, __HIP_MEMORY_SCOPE_AGENT); }
; __device__ __forceinline__ unsigned xb_add(unsigned* p, unsigned v) { return __hip_atomic_fetch_add(p, v, __ATOMIC_RELAXED, __HIP_MEMORY_SCOPE_AGENT); }
; #define XB_SPIN(cond, bar) do { unsigned _sp = 0; while (cond) { __builtin_amdgcn_s_sleep(1); \
;     if ((++_sp & 255u) == 0u) { if (xb_ld(&(bar)[XB_TMO])) break; if (_sp > XB_SPIN_CAP) { atomicAdd(&(bar)[XB_TMO], 1u); break; } } } } while (0)
; __device__ __forceinline__ void xcd_barrier(const XcdBarrier& b) {
;     ...
;             const unsigned og = xb_add(&bar[XB_TOP], 1u);
;             const unsigned tg = og / nx;
;             if (og + 1u == (tg + 1u) * nx) xb_add(&bar[XB_TOPGEN], 1u);
;             else XB_SPIN(xb_ld(&bar[XB_TOPGEN]) == tg, bar);
;             __builtin_amdgcn_fence(__ATOMIC_ACQUIRE, "agent");
;             xb_add(&bar[XB_XGEN(b.x)], 1u);
;             asm volatile("s_waitcnt vmcnt(0)" ::: "memory");
.LBB0_382:
	s_or_b64 exec, exec, s[8:9]
	s_and_saveexec_b64 s[8:9], s[12:13]
	s_cbranch_execz .LBB0_384
	v_mov_b32_e32 v1, 1
	global_atomic_add v[2:3], v1, off
	v_mov_b32_e32 v2, 0x2400
	global_atomic_add v2, v1, s[90:91]
	v_mov_b32_e32 v2, 0x2500
	global_atomic_add v2, v1, s[90:91]
	v_mov_b32_e32 v2, 0x2600
	global_atomic_add v2, v1, s[90:91]
	v_mov_b32_e32 v2, 0x2700
	global_atomic_add v2, v1, s[90:91]
	v_mov_b32_e32 v2, 0x2800
	global_atomic_add v2, v1, s[90:91]
	v_mov_b32_e32 v2, 0x2900
	global_atomic_add v2, v1, s[90:91]
	v_mov_b32_e32 v2, 0x2a00
	global_atomic_add v2, v1, s[90:91]
	v_mov_b32_e32 v2, 0x2b00
	global_atomic_add v2, v1, s[90:91]
	v_mov_b32_e32 v2, 0x2c00
	global_atomic_add v2, v1, s[90:91]
	v_mov_b32_e32 v2, 0x2d00
	global_atomic_add v2, v1, s[90:91]
	v_mov_b32_e32 v2, 0x2e00
	global_atomic_add v2, v1, s[90:91]
	v_mov_b32_e32 v2, 0x2f00
	global_atomic_add v2, v1, s[90:91]
	v_mov_b32_e32 v2, 0x3000
	global_atomic_add v2, v1, s[90:91]
	v_mov_b32_e32 v2, 0x3100
	global_atomic_add v2, v1, s[90:91]
	v_mov_b32_e32 v2, 0x3200
	global_atomic_add v2, v1, s[90:91]
	v_mov_b32_e32 v2, 0x3300
	global_atomic_add v2, v1, s[90:91]
.LBB0_384:
	s_or_b64 exec, exec, s[8:9]
	s_mov_b64 s[8:9], exec
	v_mbcnt_lo_u32_b32 v1, s8, 0
	v_mbcnt_hi_u32_b32 v1, s9, v1
	v_cmp_eq_u32_e32 vcc, 0, v1
	s_and_saveexec_b64 s[10:11], vcc
	s_cbranch_execz .LBB0_386
	s_bcnt1_i32_b64 s2, s[8:9]
	v_mov_b32_e32 v1, 0x2000
	v_mov_b32_e32 v2, s2
.LBB0_386:
	s_or_b64 exec, exec, s[10:11]

; __device__ __forceinline__ unsigned xb_ld(unsigned* p)              { return __hip_atomic_load(p, __ATOMIC_RELAXED, __HIP_MEMORY_SCOPE_AGENT); }
; __device__ __forceinline__ unsigned xb_add(unsigned* p, unsigned v) { return __hip_atomic_fetch_add(p, v, __ATOMIC_RELAXED, __HIP_MEMORY_SCOPE_AGENT); }
; #define XB_SPIN(cond, bar) do { unsigned _sp = 0; while (cond) { __builtin_amdgcn_s_sleep(1); \
;     if ((++_sp & 255u) == 0u) { if (xb_ld(&(bar)[XB_TMO])) break; if (_sp > XB_SPIN_CAP) { atomicAdd(&(bar)[XB_TMO], 1u); break; } } } } while (0)
; __device__ __forceinline__ void xcd_barrier(const XcdBarrier& b) {
;     ...
;             const unsigned og = xb_add(&bar[XB_TOP], 1u);
;             const unsigned tg = og / nx;
;             if (og + 1u == (tg + 1u) * nx) xb_add(&bar[XB_TOPGEN], 1u);
;             else XB_SPIN(xb_ld(&bar[XB_TOPGEN]) == tg, bar);
;             __builtin_amdgcn_fence(__ATOMIC_ACQUIRE, "agent");
;             xb_add(&bar[XB_XGEN(b.x)], 1u);
;             asm volatile("s_waitcnt vmcnt(0)" ::: "memory");
.LBB0_540:
	s_or_b64 exec, exec, s[6:7]
	s_and_saveexec_b64 s[6:7], s[10:11]
	s_cbranch_execz .LBB0_542
	v_mov_b32_e32 v1, 1
	global_atomic_add v[2:3], v1, off
	v_mov_b32_e32 v2, 0x2400
	global_atomic_add v2, v1, s[90:91]
	v_mov_b32_e32 v2, 0x2500
	global_atomic_add v2, v1, s[90:91]
	v_mov_b32_e32 v2, 0x2600
	global_atomic_add v2, v1, s[90:91]
	v_mov_b32_e32 v2, 0x2700
	global_atomic_add v2, v1, s[90:91]
	v_mov_b32_e32 v2, 0x2800
	global_atomic_add v2, v1, s[90:91]
	v_mov_b32_e32 v2, 0x2900
	global_atomic_add v2, v1, s[90:91]
	v_mov_b32_e32 v2, 0x2a00
	global_atomic_add v2, v1, s[90:91]
	v_mov_b32_e32 v2, 0x2b00
	global_atomic_add v2, v1, s[90:91]
	v_mov_b32_e32 v2, 0x2c00
	global_atomic_add v2, v1, s[90:91]
	v_mov_b32_e32 v2, 0x2d00
	global_atomic_add v2, v1, s[90:91]
	v_mov_b32_e32 v2, 0x2e00
	global_atomic_add v2, v1, s[90:91]
	v_mov_b32_e32 v2, 0x2f00
	global_atomic_add v2, v1, s[90:91]
	v_mov_b32_e32 v2, 0x3000
	global_atomic_add v2, v1, s[90:91]
	v_mov_b32_e32 v2, 0x3100
	global_atomic_add v2, v1, s[90:91]
	v_mov_b32_e32 v2, 0x3200
	global_atomic_add v2, v1, s[90:91]
	v_mov_b32_e32 v2, 0x3300
	global_atomic_add v2, v1, s[90:91]
.LBB0_542:
	s_or_b64 exec, exec, s[6:7]
	s_mov_b64 s[6:7], exec
	v_mbcnt_lo_u32_b32 v1, s6, 0
	v_mbcnt_hi_u32_b32 v1, s7, v1
	v_cmp_eq_u32_e32 vcc, 0, v1
	s_and_saveexec_b64 s[8:9], vcc
	s_cbranch_execz .LBB0_544
	s_bcnt1_i32_b64 s2, s[6:7]
	v_mov_b32_e32 v1, 0x2000
	v_mov_b32_e32 v2, s2
.LBB0_544:
	s_or_b64 exec, exec, s[8:9]

; __device__ __forceinline__ unsigned xb_add(unsigned* p, unsigned v) { return __hip_atomic_fetch_add(p, v, __ATOMIC_RELAXED, __HIP_MEMORY_SCOPE_AGENT); }
; __device__ __forceinline__ void xcd_barrier(const XcdBarrier& b) {
;     ...
;             __builtin_amdgcn_fence(__ATOMIC_ACQUIRE, "agent");
;             xb_add(&bar[XB_XGEN(b.x)], 1u);
;             asm volatile("s_waitcnt vmcnt(0)" ::: "memory");
.LBB0_610:
	s_or_b64 exec, exec, s[8:9]
	s_mov_b64 s[8:9], exec
	v_mbcnt_lo_u32_b32 v1, s8, 0
	v_mbcnt_hi_u32_b32 v1, s9, v1
	v_cmp_eq_u32_e32 vcc, 0, v1
	s_and_saveexec_b64 s[10:11], vcc
	s_cbranch_execz .LBB0_612
	s_bcnt1_i32_b64 s2, s[8:9]
	v_mov_b32_e32 v1, 0x2000
	v_mov_b32_e32 v2, s2
.LBB0_612:
	s_or_b64 exec, exec, s[10:11]

; __device__ __forceinline__ unsigned xb_add(unsigned* p, unsigned v) { return __hip_atomic_fetch_add(p, v, __ATOMIC_RELAXED, __HIP_MEMORY_SCOPE_AGENT); }
; __device__ __forceinline__ void xcd_barrier(const XcdBarrier& b) {
;     ...
;             __builtin_amdgcn_fence(__ATOMIC_ACQUIRE, "agent");
;             xb_add(&bar[XB_XGEN(b.x)], 1u);
;             asm volatile("s_waitcnt vmcnt(0)" ::: "memory");
.LBB0_707:
	s_or_b64 exec, exec, s[8:9]
	s_mov_b64 s[8:9], exec
	v_mbcnt_lo_u32_b32 v1, s8, 0
	v_mbcnt_hi_u32_b32 v1, s9, v1
	v_cmp_eq_u32_e32 vcc, 0, v1
	s_and_saveexec_b64 s[10:11], vcc
	s_cbranch_execz .LBB0_709
	s_bcnt1_i32_b64 s2, s[8:9]
	v_mov_b32_e32 v1, 0x2000
	v_mov_b32_e32 v2, s2
.LBB0_709:
	s_or_b64 exec, exec, s[10:11]

; __device__ __forceinline__ unsigned xb_add(unsigned* p, unsigned v) { return __hip_atomic_fetch_add(p, v, __ATOMIC_RELAXED, __HIP_MEMORY_SCOPE_AGENT); }
; __device__ __forceinline__ void xcd_barrier(const XcdBarrier& b) {
;     ...
;             __builtin_amdgcn_fence(__ATOMIC_ACQUIRE, "agent");
;             xb_add(&bar[XB_XGEN(b.x)], 1u);
;             asm volatile("s_waitcnt vmcnt(0)" ::: "memory");
.LBB0_829:
	s_or_b64 exec, exec, s[8:9]
	s_mov_b64 s[8:9], exec
	v_mbcnt_lo_u32_b32 v1, s8, 0
	v_mbcnt_hi_u32_b32 v1, s9, v1
	v_cmp_eq_u32_e32 vcc, 0, v1
	s_and_saveexec_b64 s[10:11], vcc
	s_cbranch_execz .LBB0_831
	s_bcnt1_i32_b64 s2, s[8:9]
	v_mov_b32_e32 v1, 0x2000
	v_mov_b32_e32 v2, s2
.LBB0_831:
	s_or_b64 exec, exec, s[10:11]

; __device__ __forceinline__ unsigned xb_add(unsigned* p, unsigned v) { return __hip_atomic_fetch_add(p, v, __ATOMIC_RELAXED, __HIP_MEMORY_SCOPE_AGENT); }
; __device__ __forceinline__ void xcd_barrier(const XcdBarrier& b) {
;     ...
;             __builtin_amdgcn_fence(__ATOMIC_ACQUIRE, "agent");
;             xb_add(&bar[XB_XGEN(b.x)], 1u);
;             asm volatile("s_waitcnt vmcnt(0)" ::: "memory");
.LBB0_930:
	s_or_b64 exec, exec, s[6:7]
	s_mov_b64 s[6:7], exec
	v_mbcnt_lo_u32_b32 v1, s6, 0
	v_mbcnt_hi_u32_b32 v1, s7, v1
	v_cmp_eq_u32_e32 vcc, 0, v1
	s_and_saveexec_b64 s[8:9], vcc
	s_cbranch_execz .LBB0_932
	s_bcnt1_i32_b64 s2, s[6:7]
	v_mov_b32_e32 v1, 0x2000
	v_mov_b32_e32 v2, s2
.LBB0_932:
	s_or_b64 exec, exec, s[8:9]

; __device__ __forceinline__ unsigned xb_add(unsigned* p, unsigned v) { return __hip_atomic_fetch_add(p, v, __ATOMIC_RELAXED, __HIP_MEMORY_SCOPE_AGENT); }
; __device__ __forceinline__ void xcd_barrier(const XcdBarrier& b) {
;     ...
;             __builtin_amdgcn_fence(__ATOMIC_ACQUIRE, "agent");
;             xb_add(&bar[XB_XGEN(b.x)], 1u);
;             asm volatile("s_waitcnt vmcnt(0)" ::: "memory");
.LBB0_1075:
	s_or_b64 exec, exec, s[8:9]
	s_mov_b64 s[8:9], exec
	v_mbcnt_lo_u32_b32 v1, s8, 0
	v_mbcnt_hi_u32_b32 v1, s9, v1
	v_cmp_eq_u32_e32 vcc, 0, v1
	s_and_saveexec_b64 s[10:11], vcc
	s_cbranch_execz .LBB0_1077
	s_bcnt1_i32_b64 s2, s[8:9]
	v_mov_b32_e32 v1, 0x2000
	v_mov_b32_e32 v2, s2
.LBB0_1077:
	s_or_b64 exec, exec, s[10:11]

; __device__ __forceinline__ unsigned xb_add(unsigned* p, unsigned v) { return __hip_atomic_fetch_add(p, v, __ATOMIC_RELAXED, __HIP_MEMORY_SCOPE_AGENT); }
; __device__ __forceinline__ void xcd_barrier(const XcdBarrier& b) {
;     ...
;             __builtin_amdgcn_fence(__ATOMIC_ACQUIRE, "agent");
;             xb_add(&bar[XB_XGEN(b.x)], 1u);
;             asm volatile("s_waitcnt vmcnt(0)" ::: "memory");
.LBB0_1233:
	s_or_b64 exec, exec, s[6:7]
	s_mov_b64 s[6:7], exec
	v_mbcnt_lo_u32_b32 v1, s6, 0
	v_mbcnt_hi_u32_b32 v1, s7, v1
	v_cmp_eq_u32_e32 vcc, 0, v1
	s_and_saveexec_b64 s[8:9], vcc
	s_cbranch_execz .LBB0_1235
	s_bcnt1_i32_b64 s2, s[6:7]
	v_mov_b32_e32 v1, 0x2000
	v_mov_b32_e32 v2, s2
.LBB0_1235:
	s_or_b64 exec, exec, s[8:9]

; __device__ __forceinline__ unsigned xb_add(unsigned* p, unsigned v) { return __hip_atomic_fetch_add(p, v, __ATOMIC_RELAXED, __HIP_MEMORY_SCOPE_AGENT); }
; __device__ __forceinline__ void xcd_barrier(const XcdBarrier& b) {
;     ...
;             __builtin_amdgcn_fence(__ATOMIC_ACQUIRE, "agent");
;             xb_add(&bar[XB_XGEN(b.x)], 1u);
;             asm volatile("s_waitcnt vmcnt(0)" ::: "memory");
.LBB0_1300:
	s_or_b64 exec, exec, s[8:9]
	s_mov_b64 s[8:9], exec
	v_mbcnt_lo_u32_b32 v1, s8, 0
	v_mbcnt_hi_u32_b32 v1, s9, v1
	v_cmp_eq_u32_e32 vcc, 0, v1
	s_and_saveexec_b64 s[10:11], vcc
	s_cbranch_execz .LBB0_1302
	s_bcnt1_i32_b64 s2, s[8:9]
	v_mov_b32_e32 v1, 0x2000
	v_mov_b32_e32 v2, s2
.LBB0_1302:
	s_or_b64 exec, exec, s[10:11]

; __device__ __forceinline__ unsigned xb_add(unsigned* p, unsigned v) { return __hip_atomic_fetch_add(p, v, __ATOMIC_RELAXED, __HIP_MEMORY_SCOPE_AGENT); }
; __device__ __forceinline__ void xcd_barrier(const XcdBarrier& b) {
;     ...
;             __builtin_amdgcn_fence(__ATOMIC_ACQUIRE, "agent");
;             xb_add(&bar[XB_XGEN(b.x)], 1u);
;             asm volatile("s_waitcnt vmcnt(0)" ::: "memory");
.LBB0_1397:
	s_or_b64 exec, exec, s[8:9]
	s_mov_b64 s[8:9], exec
	v_mbcnt_lo_u32_b32 v1, s8, 0
	v_mbcnt_hi_u32_b32 v1, s9, v1
	v_cmp_eq_u32_e32 vcc, 0, v1
	s_and_saveexec_b64 s[10:11], vcc
	s_cbranch_execz .LBB0_1399
	s_bcnt1_i32_b64 s2, s[8:9]
	v_mov_b32_e32 v1, 0x2000
	v_mov_b32_e32 v2, s2
.LBB0_1399:
	s_or_b64 exec, exec, s[10:11]

; __device__ __forceinline__ unsigned xb_add(unsigned* p, unsigned v) { return __hip_atomic_fetch_add(p, v, __ATOMIC_RELAXED, __HIP_MEMORY_SCOPE_AGENT); }
; __device__ __forceinline__ void xcd_barrier(const XcdBarrier& b) {
;     ...
;             __builtin_amdgcn_fence(__ATOMIC_ACQUIRE, "agent");
;             xb_add(&bar[XB_XGEN(b.x)], 1u);
;             asm volatile("s_waitcnt vmcnt(0)" ::: "memory");
.LBB0_1489:
	s_or_b64 exec, exec, s[8:9]
	s_mov_b64 s[8:9], exec
	v_mbcnt_lo_u32_b32 v1, s8, 0
	v_mbcnt_hi_u32_b32 v1, s9, v1
	v_cmp_eq_u32_e32 vcc, 0, v1
	s_and_saveexec_b64 s[10:11], vcc
	s_cbranch_execz .LBB0_1491
	s_bcnt1_i32_b64 s2, s[8:9]
	v_mov_b32_e32 v1, 0x2000
	v_mov_b32_e32 v2, s2
.LBB0_1491:
	s_or_b64 exec, exec, s[10:11]

; __device__ __forceinline__ unsigned xb_ld(unsigned* p)              { return __hip_atomic_load(p, __ATOMIC_RELAXED, __HIP_MEMORY_SCOPE_AGENT); }
; __device__ __forceinline__ unsigned xb_add(unsigned* p, unsigned v) { return __hip_atomic_fetch_add(p, v, __ATOMIC_RELAXED, __HIP_MEMORY_SCOPE_AGENT); }
; #define XB_SPIN(cond, bar) do { unsigned _sp = 0; while (cond) { __builtin_amdgcn_s_sleep(1); \
;     if ((++_sp & 255u) == 0u) { if (xb_ld(&(bar)[XB_TMO])) break; if (_sp > XB_SPIN_CAP) { atomicAdd(&(bar)[XB_TMO], 1u); break; } } } } while (0)
; __device__ __forceinline__ void xcd_barrier(const XcdBarrier& b) {
;     ...
;             const unsigned og = xb_add(&bar[XB_TOP], 1u);
;             const unsigned tg = og / nx;
;             if (og + 1u == (tg + 1u) * nx) xb_add(&bar[XB_TOPGEN], 1u);
;             else XB_SPIN(xb_ld(&bar[XB_TOPGEN]) == tg, bar);
;             __builtin_amdgcn_fence(__ATOMIC_ACQUIRE, "agent");
;             xb_add(&bar[XB_XGEN(b.x)], 1u);
;             asm volatile("s_waitcnt vmcnt(0)" ::: "memory");
.LBB0_1702:
	s_or_b64 exec, exec, s[10:11]
	s_and_saveexec_b64 s[10:11], s[24:25]
	s_cbranch_execz .LBB0_1704
	v_mov_b32_e32 v1, 1
	global_atomic_add v[2:3], v1, off
	v_mov_b32_e32 v2, 0x2400
	global_atomic_add v2, v1, s[90:91]
	v_mov_b32_e32 v2, 0x2500
	global_atomic_add v2, v1, s[90:91]
	v_mov_b32_e32 v2, 0x2600
	global_atomic_add v2, v1, s[90:91]
	v_mov_b32_e32 v2, 0x2700
	global_atomic_add v2, v1, s[90:91]
	v_mov_b32_e32 v2, 0x2800
	global_atomic_add v2, v1, s[90:91]
	v_mov_b32_e32 v2, 0x2900
	global_atomic_add v2, v1, s[90:91]
	v_mov_b32_e32 v2, 0x2a00
	global_atomic_add v2, v1, s[90:91]
	v_mov_b32_e32 v2, 0x2b00
	global_atomic_add v2, v1, s[90:91]
	v_mov_b32_e32 v2, 0x2c00
	global_atomic_add v2, v1, s[90:91]
	v_mov_b32_e32 v2, 0x2d00
	global_atomic_add v2, v1, s[90:91]
	v_mov_b32_e32 v2, 0x2e00
	global_atomic_add v2, v1, s[90:91]
	v_mov_b32_e32 v2, 0x2f00
	global_atomic_add v2, v1, s[90:91]
	v_mov_b32_e32 v2, 0x3000
	global_atomic_add v2, v1, s[90:91]
	v_mov_b32_e32 v2, 0x3100
	global_atomic_add v2, v1, s[90:91]
	v_mov_b32_e32 v2, 0x3200
	global_atomic_add v2, v1, s[90:91]
	v_mov_b32_e32 v2, 0x3300
	global_atomic_add v2, v1, s[90:91]
.LBB0_1704:
	s_or_b64 exec, exec, s[10:11]
	s_mov_b64 s[10:11], exec
	v_mbcnt_lo_u32_b32 v1, s10, 0
	v_mbcnt_hi_u32_b32 v1, s11, v1
	v_cmp_eq_u32_e32 vcc, 0, v1
	s_and_saveexec_b64 s[22:23], vcc
	s_cbranch_execz .LBB0_1706
	s_bcnt1_i32_b64 s2, s[10:11]
	v_mov_b32_e32 v1, 0x2000
	v_mov_b32_e32 v2, s2
.LBB0_1706:
	s_or_b64 exec, exec, s[22:23]

; __device__ __forceinline__ unsigned xb_ld(unsigned* p)              { return __hip_atomic_load(p, __ATOMIC_RELAXED, __HIP_MEMORY_SCOPE_AGENT); }
; __device__ __forceinline__ unsigned xb_add(unsigned* p, unsigned v) { return __hip_atomic_fetch_add(p, v, __ATOMIC_RELAXED, __HIP_MEMORY_SCOPE_AGENT); }
; #define XB_SPIN(cond, bar) do { unsigned _sp = 0; while (cond) { __builtin_amdgcn_s_sleep(1); \
;     if ((++_sp & 255u) == 0u) { if (xb_ld(&(bar)[XB_TMO])) break; if (_sp > XB_SPIN_CAP) { atomicAdd(&(bar)[XB_TMO], 1u); break; } } } } while (0)
; __device__ __forceinline__ void xcd_barrier(const XcdBarrier& b) {
;     ...
;             const unsigned og = xb_add(&bar[XB_TOP], 1u);
;             const unsigned tg = og / nx;
;             if (og + 1u == (tg + 1u) * nx) xb_add(&bar[XB_TOPGEN], 1u);
;             else XB_SPIN(xb_ld(&bar[XB_TOPGEN]) == tg, bar);
;             __builtin_amdgcn_fence(__ATOMIC_ACQUIRE, "agent");
;             xb_add(&bar[XB_XGEN(b.x)], 1u);
;             asm volatile("s_waitcnt vmcnt(0)" ::: "memory");
.LBB0_1795:
	s_or_b64 exec, exec, s[8:9]
	s_and_saveexec_b64 s[8:9], s[18:19]
	s_cbranch_execz .LBB0_1797
	v_mov_b32_e32 v1, 1
	global_atomic_add v[2:3], v1, off
	v_mov_b32_e32 v2, 0x2400
	global_atomic_add v2, v1, s[90:91]
	v_mov_b32_e32 v2, 0x2500
	global_atomic_add v2, v1, s[90:91]
	v_mov_b32_e32 v2, 0x2600
	global_atomic_add v2, v1, s[90:91]
	v_mov_b32_e32 v2, 0x2700
	global_atomic_add v2, v1, s[90:91]
	v_mov_b32_e32 v2, 0x2800
	global_atomic_add v2, v1, s[90:91]
	v_mov_b32_e32 v2, 0x2900
	global_atomic_add v2, v1, s[90:91]
	v_mov_b32_e32 v2, 0x2a00
	global_atomic_add v2, v1, s[90:91]
	v_mov_b32_e32 v2, 0x2b00
	global_atomic_add v2, v1, s[90:91]
	v_mov_b32_e32 v2, 0x2c00
	global_atomic_add v2, v1, s[90:91]
	v_mov_b32_e32 v2, 0x2d00
	global_atomic_add v2, v1, s[90:91]
	v_mov_b32_e32 v2, 0x2e00
	global_atomic_add v2, v1, s[90:91]
	v_mov_b32_e32 v2, 0x2f00
	global_atomic_add v2, v1, s[90:91]
	v_mov_b32_e32 v2, 0x3000
	global_atomic_add v2, v1, s[90:91]
	v_mov_b32_e32 v2, 0x3100
	global_atomic_add v2, v1, s[90:91]
	v_mov_b32_e32 v2, 0x3200
	global_atomic_add v2, v1, s[90:91]
	v_mov_b32_e32 v2, 0x3300
	global_atomic_add v2, v1, s[90:91]
.LBB0_1797:
	s_or_b64 exec, exec, s[8:9]
	s_mov_b64 s[8:9], exec
	v_mbcnt_lo_u32_b32 v1, s8, 0
	v_mbcnt_hi_u32_b32 v1, s9, v1
	v_cmp_eq_u32_e32 vcc, 0, v1
	s_and_saveexec_b64 s[10:11], vcc
	s_cbranch_execz .LBB0_1799
	s_bcnt1_i32_b64 s2, s[8:9]
	v_mov_b32_e32 v1, 0x2000
	v_mov_b32_e32 v2, s2
.LBB0_1799:
	s_or_b64 exec, exec, s[10:11]

; __device__ __forceinline__ unsigned xb_ld(unsigned* p)              { return __hip_atomic_load(p, __ATOMIC_RELAXED, __HIP_MEMORY_SCOPE_AGENT); }
; __device__ __forceinline__ unsigned xb_add(unsigned* p, unsigned v) { return __hip_atomic_fetch_add(p, v, __ATOMIC_RELAXED, __HIP_MEMORY_SCOPE_AGENT); }
; #define XB_SPIN(cond, bar) do { unsigned _sp = 0; while (cond) { __builtin_amdgcn_s_sleep(1); \
;     if ((++_sp & 255u) == 0u) { if (xb_ld(&(bar)[XB_TMO])) break; if (_sp > XB_SPIN_CAP) { atomicAdd(&(bar)[XB_TMO], 1u); break; } } } } while (0)
; __device__ __forceinline__ void xcd_barrier(const XcdBarrier& b) {
;     ...
;             const unsigned og = xb_add(&bar[XB_TOP], 1u);
;             const unsigned tg = og / nx;
;             if (og + 1u == (tg + 1u) * nx) xb_add(&bar[XB_TOPGEN], 1u);
;             else XB_SPIN(xb_ld(&bar[XB_TOPGEN]) == tg, bar);
;             __builtin_amdgcn_fence(__ATOMIC_ACQUIRE, "agent");
;             xb_add(&bar[XB_XGEN(b.x)], 1u);
;             asm volatile("s_waitcnt vmcnt(0)" ::: "memory");
.LBB0_1899:
	s_or_b64 exec, exec, s[10:11]
	s_and_saveexec_b64 s[10:11], s[16:17]
	s_cbranch_execz .LBB0_1901
	v_mov_b32_e32 v1, 1
	global_atomic_add v[2:3], v1, off
	v_mov_b32_e32 v2, 0x2400
	global_atomic_add v2, v1, s[90:91]
	v_mov_b32_e32 v2, 0x2500
	global_atomic_add v2, v1, s[90:91]
	v_mov_b32_e32 v2, 0x2600
	global_atomic_add v2, v1, s[90:91]
	v_mov_b32_e32 v2, 0x2700
	global_atomic_add v2, v1, s[90:91]
	v_mov_b32_e32 v2, 0x2800
	global_atomic_add v2, v1, s[90:91]
	v_mov_b32_e32 v2, 0x2900
	global_atomic_add v2, v1, s[90:91]
	v_mov_b32_e32 v2, 0x2a00
	global_atomic_add v2, v1, s[90:91]
	v_mov_b32_e32 v2, 0x2b00
	global_atomic_add v2, v1, s[90:91]
	v_mov_b32_e32 v2, 0x2c00
	global_atomic_add v2, v1, s[90:91]
	v_mov_b32_e32 v2, 0x2d00
	global_atomic_add v2, v1, s[90:91]
	v_mov_b32_e32 v2, 0x2e00
	global_atomic_add v2, v1, s[90:91]
	v_mov_b32_e32 v2, 0x2f00
	global_atomic_add v2, v1, s[90:91]
	v_mov_b32_e32 v2, 0x3000
	global_atomic_add v2, v1, s[90:91]
	v_mov_b32_e32 v2, 0x3100
	global_atomic_add v2, v1, s[90:91]
	v_mov_b32_e32 v2, 0x3200
	global_atomic_add v2, v1, s[90:91]
	v_mov_b32_e32 v2, 0x3300
	global_atomic_add v2, v1, s[90:91]
.LBB0_1901:
	s_or_b64 exec, exec, s[10:11]
	s_mov_b64 s[10:11], exec
	v_mbcnt_lo_u32_b32 v1, s10, 0
	v_mbcnt_hi_u32_b32 v1, s11, v1
	v_cmp_eq_u32_e32 vcc, 0, v1
	s_and_saveexec_b64 s[14:15], vcc
	s_cbranch_execz .LBB0_1903
	s_bcnt1_i32_b64 s2, s[10:11]
	v_mov_b32_e32 v1, 0x2000
	v_mov_b32_e32 v2, s2
.LBB0_1903:
	s_or_b64 exec, exec, s[14:15]
